# NA: last key tile of a unit goes through the main tile loop (one more trip) instead of the separate tail with serial per-element mask code; dead tail removed
# speedup vs baseline: 1.0003x; 1.0003x over previous
.LBB0_601:
	v_cndmask_b32_e64 v184, v98, v184, s[72:73]
	v_mul_f32_e32 v98, 0xbe0293ee, v184
	v_fmamk_f32 v82, v82, 0x3e0293ee, v98
	v_fmamk_f32 v83, v83, 0x3e0293ee, v98
	v_fmamk_f32 v84, v84, 0x3e0293ee, v98
	v_fmamk_f32 v85, v85, 0x3e0293ee, v98
	v_fmamk_f32 v86, v86, 0x3e0293ee, v98
	v_fmamk_f32 v87, v87, 0x3e0293ee, v98
	v_fmamk_f32 v88, v88, 0x3e0293ee, v98
	v_fmamk_f32 v89, v89, 0x3e0293ee, v98
	v_fmamk_f32 v90, v90, 0x3e0293ee, v98
	v_fmamk_f32 v91, v91, 0x3e0293ee, v98
	v_fmamk_f32 v92, v92, 0x3e0293ee, v98
	v_fmamk_f32 v93, v93, 0x3e0293ee, v98
	v_fmamk_f32 v94, v94, 0x3e0293ee, v98
	v_fmamk_f32 v95, v95, 0x3e0293ee, v98
	v_fmamk_f32 v96, v96, 0x3e0293ee, v98
	v_fmamk_f32 v97, v97, 0x3e0293ee, v98
	v_fmamk_f32 v0, v0, 0x3e0293ee, v98
	v_fmamk_f32 v66, v66, 0x3e0293ee, v98
	v_fmamk_f32 v67, v67, 0x3e0293ee, v98
	v_fmamk_f32 v68, v68, 0x3e0293ee, v98
	v_fmamk_f32 v69, v69, 0x3e0293ee, v98
	v_fmamk_f32 v70, v70, 0x3e0293ee, v98
	v_fmamk_f32 v71, v71, 0x3e0293ee, v98
	v_fmamk_f32 v72, v72, 0x3e0293ee, v98
	v_fmamk_f32 v73, v73, 0x3e0293ee, v98
	v_fmamk_f32 v74, v74, 0x3e0293ee, v98
	v_fmamk_f32 v75, v75, 0x3e0293ee, v98
	v_fmamk_f32 v76, v76, 0x3e0293ee, v98
	v_fmamk_f32 v77, v77, 0x3e0293ee, v98
	v_fmamk_f32 v78, v78, 0x3e0293ee, v98
	v_fmamk_f32 v79, v79, 0x3e0293ee, v98
	v_fmac_f32_e32 v98, 0x3e0293ee, v80
	v_exp_f32_e32 v80, v82
	v_exp_f32_e32 v82, v83
	v_exp_f32_e32 v83, v84
	v_exp_f32_e32 v84, v85
	v_exp_f32_e32 v85, v86
	v_exp_f32_e32 v86, v87
	v_exp_f32_e32 v87, v88
	v_exp_f32_e32 v88, v89
	v_exp_f32_e32 v89, v90
	v_exp_f32_e32 v90, v91
	v_exp_f32_e32 v91, v92
	v_exp_f32_e32 v92, v93
	v_exp_f32_e32 v93, v94
	v_exp_f32_e32 v94, v95
	v_exp_f32_e32 v95, v96
	v_exp_f32_e32 v96, v97
	v_exp_f32_e32 v97, v0
	v_add_f32_e32 v0, 0, v80
	v_add_f32_e32 v0, v82, v0
	v_add_f32_e32 v0, v83, v0
	v_add_f32_e32 v0, v84, v0
	v_add_f32_e32 v0, v85, v0
	v_add_f32_e32 v0, v86, v0
	v_add_f32_e32 v0, v87, v0
	v_add_f32_e32 v0, v88, v0
	v_add_f32_e32 v0, v89, v0
	v_add_f32_e32 v0, v90, v0
	v_add_f32_e32 v0, v91, v0
	v_add_f32_e32 v0, v92, v0
	v_add_f32_e32 v0, v93, v0
	v_exp_f32_e32 v99, v66
	v_add_f32_e32 v0, v94, v0
	v_exp_f32_e32 v100, v67
	v_add_f32_e32 v0, v95, v0
	v_exp_f32_e32 v101, v68
	v_add_f32_e32 v0, v96, v0
	v_exp_f32_e32 v102, v69
	v_add_f32_e32 v0, v97, v0
	v_exp_f32_e32 v103, v70
	v_add_f32_e32 v0, v99, v0
	v_exp_f32_e32 v104, v71
	v_add_f32_e32 v0, v100, v0
	v_exp_f32_e32 v105, v72
	v_add_f32_e32 v0, v101, v0
	v_exp_f32_e32 v106, v73
	v_add_f32_e32 v0, v102, v0
	v_exp_f32_e32 v107, v74
	v_add_f32_e32 v0, v103, v0
	v_exp_f32_e32 v108, v75
	v_add_f32_e32 v0, v104, v0
	v_exp_f32_e32 v109, v76
	v_add_f32_e32 v0, v105, v0
	v_exp_f32_e32 v110, v77
	v_add_f32_e32 v0, v106, v0
	v_exp_f32_e32 v111, v78
	v_add_f32_e32 v0, v107, v0
	v_exp_f32_e32 v112, v79
	v_add_f32_e32 v0, v108, v0
	v_exp_f32_e32 v98, v98
	v_add_f32_e32 v0, v109, v0
	v_add_f32_e32 v0, v110, v0
	v_add_f32_e32 v0, v111, v0
	v_add_f32_e32 v0, v112, v0
	v_add_f32_e32 v0, v98, v0
	v_mov_b32_e32 v66, v0
	s_nop 1
	v_permlane32_swap_b32_e32 v0, v66
	v_add_f32_e32 v0, v0, v66
	v_fmac_f32_e32 v0, v200, v81
	v_cvt_pk_bf16_f32 v66, v80, v82
	v_cvt_pk_bf16_f32 v67, v83, v84
	v_cvt_pk_bf16_f32 v68, v85, v86
	v_cvt_pk_bf16_f32 v69, v87, v88
	v_cvt_pk_bf16_f32 v70, v89, v90
	v_cvt_pk_bf16_f32 v71, v91, v92
	v_cvt_pk_bf16_f32 v72, v93, v94
	v_cvt_pk_bf16_f32 v73, v95, v96
	v_cvt_pk_bf16_f32 v74, v97, v99
	v_cvt_pk_bf16_f32 v75, v100, v101
	v_cvt_pk_bf16_f32 v76, v102, v103
	v_cvt_pk_bf16_f32 v77, v104, v105
	v_cvt_pk_bf16_f32 v78, v106, v107
	v_cvt_pk_bf16_f32 v79, v108, v109
	v_cvt_pk_bf16_f32 v80, v110, v111
	v_cvt_pk_bf16_f32 v81, v112, v98
	s_nop 0
	v_permlane32_swap_b32_e32 v66, v68
	v_permlane32_swap_b32_e32 v67, v69
	v_permlane32_swap_b32_e32 v70, v72
	v_permlane32_swap_b32_e32 v71, v73
	v_permlane32_swap_b32_e32 v74, v76
	v_permlane32_swap_b32_e32 v75, v77
	v_permlane32_swap_b32_e32 v78, v80
	v_permlane32_swap_b32_e32 v79, v81
	v_add_u32_e32 v98, s1, v182
	ds_read_b64_tr_b16 v[82:83], v98 offset:0
	ds_read_b64_tr_b16 v[84:85], v98 offset:0x800
	ds_read_b64_tr_b16 v[86:87], v98 offset:0x1000
	ds_read_b64_tr_b16 v[88:89], v98 offset:0x1800
	ds_read_b64_tr_b16 v[90:91], v98 offset:0x2000
	ds_read_b64_tr_b16 v[92:93], v98 offset:0x2800
	ds_read_b64_tr_b16 v[94:95], v98 offset:0x3000
	ds_read_b64_tr_b16 v[96:97], v98 offset:0x3800
	s_waitcnt lgkmcnt(0)
	s_nop 0
	v_mfma_f32_32x32x16_bf16 v[50:65], v[66:69], v[82:85], v[50:65]
	ds_read_b64_tr_b16 v[82:83], v98 offset:0x200
	ds_read_b64_tr_b16 v[84:85], v98 offset:0xa00
	v_mfma_f32_32x32x16_bf16 v[50:65], v[70:73], v[86:89], v[50:65]
	ds_read_b64_tr_b16 v[86:87], v98 offset:0x1200
	ds_read_b64_tr_b16 v[88:89], v98 offset:0x1a00
	v_mfma_f32_32x32x16_bf16 v[50:65], v[74:77], v[90:93], v[50:65]
	ds_read_b64_tr_b16 v[90:91], v98 offset:0x2200
	ds_read_b64_tr_b16 v[92:93], v98 offset:0x2a00
	v_mfma_f32_32x32x16_bf16 v[50:65], v[78:81], v[94:97], v[50:65]
	ds_read_b64_tr_b16 v[94:95], v98 offset:0x3200
	ds_read_b64_tr_b16 v[96:97], v98 offset:0x3a00
	s_waitcnt lgkmcnt(0)
	v_mfma_f32_32x32x16_bf16 v[34:49], v[66:69], v[82:85], v[34:49]
	ds_read_b64_tr_b16 v[82:83], v98 offset:0x400
	ds_read_b64_tr_b16 v[84:85], v98 offset:0xc00
	v_mfma_f32_32x32x16_bf16 v[34:49], v[70:73], v[86:89], v[34:49]
	ds_read_b64_tr_b16 v[86:87], v98 offset:0x1400
	ds_read_b64_tr_b16 v[88:89], v98 offset:0x1c00
	v_mfma_f32_32x32x16_bf16 v[34:49], v[74:77], v[90:93], v[34:49]
	ds_read_b64_tr_b16 v[90:91], v98 offset:0x2400
	ds_read_b64_tr_b16 v[92:93], v98 offset:0x2c00
	v_mfma_f32_32x32x16_bf16 v[34:49], v[78:81], v[94:97], v[34:49]
	ds_read_b64_tr_b16 v[94:95], v98 offset:0x3400
	ds_read_b64_tr_b16 v[96:97], v98 offset:0x3c00
	s_waitcnt lgkmcnt(0)
	v_mfma_f32_32x32x16_bf16 v[18:33], v[66:69], v[82:85], v[18:33]
	ds_read_b64_tr_b16 v[82:83], v98 offset:0x600
	ds_read_b64_tr_b16 v[84:85], v98 offset:0xe00
	v_mfma_f32_32x32x16_bf16 v[18:33], v[70:73], v[86:89], v[18:33]
	ds_read_b64_tr_b16 v[86:87], v98 offset:0x1600
	ds_read_b64_tr_b16 v[88:89], v98 offset:0x1e00
	v_mfma_f32_32x32x16_bf16 v[18:33], v[74:77], v[90:93], v[18:33]
	ds_read_b64_tr_b16 v[90:91], v98 offset:0x2600
	ds_read_b64_tr_b16 v[92:93], v98 offset:0x2e00
	v_mfma_f32_32x32x16_bf16 v[18:33], v[78:81], v[94:97], v[18:33]
	ds_read_b64_tr_b16 v[94:95], v98 offset:0x3600
	ds_read_b64_tr_b16 v[96:97], v98 offset:0x3e00
	s_waitcnt lgkmcnt(0)
	v_mfma_f32_32x32x16_bf16 v[2:17], v[66:69], v[82:85], v[2:17]
	s_waitcnt vmcnt(3)
	v_cvt_f32_fp8_e32 v66, v164
	v_cvt_f32_fp8_sdwa v67, v164 src0_sel:BYTE_1
	s_waitcnt vmcnt(0)
	v_cvt_pk_bf16_f32 v66, v66, v67
	v_cvt_f32_fp8_sdwa v67, v164 src0_sel:BYTE_2
	v_cvt_f32_fp8_sdwa v68, v164 src0_sel:BYTE_3
	v_cvt_pk_bf16_f32 v67, v67, v68
	v_mfma_f32_32x32x16_bf16 v[2:17], v[70:73], v[86:89], v[2:17]
	v_cvt_f32_fp8_e32 v68, v165
	v_cvt_f32_fp8_sdwa v69, v165 src0_sel:BYTE_1
	v_cvt_pk_bf16_f32 v68, v68, v69
	v_cvt_f32_fp8_sdwa v69, v165 src0_sel:BYTE_2
	v_cvt_f32_fp8_sdwa v70, v165 src0_sel:BYTE_3
	v_cvt_pk_bf16_f32 v69, v69, v70
	s_waitcnt vmcnt(2)
	v_cvt_f32_fp8_e32 v70, v162
	v_mfma_f32_32x32x16_bf16 v[2:17], v[74:77], v[90:93], v[2:17]
	v_cvt_f32_fp8_sdwa v71, v162 src0_sel:BYTE_1
	v_cvt_pk_bf16_f32 v70, v70, v71
	v_cvt_f32_fp8_sdwa v71, v162 src0_sel:BYTE_2
	v_cvt_f32_fp8_sdwa v72, v162 src0_sel:BYTE_3
	v_cvt_pk_bf16_f32 v71, v71, v72
	v_cvt_f32_fp8_e32 v72, v163
	v_cvt_f32_fp8_sdwa v73, v163 src0_sel:BYTE_1
	v_cvt_pk_bf16_f32 v72, v72, v73
	v_cvt_f32_fp8_sdwa v73, v163 src0_sel:BYTE_2
	v_cvt_f32_fp8_sdwa v74, v163 src0_sel:BYTE_3
	v_cvt_pk_bf16_f32 v73, v73, v74
	s_waitcnt vmcnt(1)
	v_mfma_f32_32x32x16_bf16 v[2:17], v[78:81], v[94:97], v[2:17]
	s_waitcnt vmcnt(0)
	v_cvt_f32_fp8_e32 v82, v160
	v_cvt_f32_fp8_sdwa v74, v160 src0_sel:BYTE_1
	v_cvt_f32_fp8_sdwa v83, v160 src0_sel:BYTE_2
	v_cvt_f32_fp8_sdwa v75, v160 src0_sel:BYTE_3
	v_mul_f32_e32 v86, v74, v74
	v_mul_f32_e32 v87, v75, v75
	v_cvt_f32_fp8_e32 v84, v161
	v_cvt_f32_fp8_sdwa v76, v161 src0_sel:BYTE_1
	v_fmac_f32_e32 v86, v82, v82
	v_fmac_f32_e32 v87, v83, v83
	v_add_f32_e32 v86, v86, v87
	v_mul_f32_e32 v87, v76, v76
	v_cvt_f32_fp8_sdwa v85, v161 src0_sel:BYTE_2
	v_cvt_f32_fp8_sdwa v77, v161 src0_sel:BYTE_3
	v_fmac_f32_e32 v87, v84, v84
	v_add_f32_e32 v86, v86, v87
	v_mul_f32_e32 v87, v77, v77
	v_fmac_f32_e32 v87, v85, v85
	v_add_f32_e32 v86, v86, v87
	s_nop 1
	s_xor_b32 s1, s1, 0x4000
	s_add_i32 s1, s1, 0
	s_add_i32 s92, s92, 1
	s_addk_i32 s3, 0x4000
	v_add_f32_dpp v86, v86, v86 quad_perm:[1,0,3,2] row_mask:0xf bank_mask:0xf
	s_nop 1
	s_add_u32 s96, s96, 0x2000
	s_addc_u32 s97, s97, 0
	s_cmp_eq_u32 s96, 0x18000
	v_add_f32_dpp v86, v86, v86 quad_perm:[2,3,0,1] row_mask:0xf bank_mask:0xf
	s_nop 1
	v_add_f32_dpp v86, v86, v86 row_half_mirror row_mask:0xf bank_mask:0xf
	s_nop 1
	s_waitcnt lgkmcnt(0)
	v_add_f32_dpp v86, v86, v86 row_mirror row_mask:0xf bank_mask:0xf
	v_fmamk_f32 v86, v86, 0x3c000000, v167
	v_rsq_f32_e32 v86, v86
	s_nop 0
	v_mul_f32_e32 v82, v86, v82
	v_mul_f32_e32 v74, v86, v74
	v_mul_f32_e32 v82, v150, v82
	v_mul_f32_e32 v74, v151, v74
	v_cvt_pk_bf16_f32 v74, v82, v74
	v_mul_f32_e32 v82, v86, v83
	v_mul_f32_e32 v75, v86, v75
	v_mul_f32_e32 v82, v152, v82
	v_mul_f32_e32 v75, v153, v75
	v_cvt_pk_bf16_f32 v75, v82, v75
	v_mul_f32_e32 v82, v86, v84
	v_mul_f32_e32 v76, v86, v76
	v_mul_f32_e32 v82, v146, v82
	v_mul_f32_e32 v76, v147, v76
	v_cvt_pk_bf16_f32 v76, v82, v76
	v_mul_f32_e32 v82, v86, v85
	v_mul_f32_e32 v77, v86, v77
	v_mul_f32_e32 v82, v148, v82
	v_mul_f32_e32 v77, v149, v77
	v_cvt_pk_bf16_f32 v77, v82, v77
	v_cvt_f32_fp8_e32 v82, v158
	v_cvt_f32_fp8_sdwa v78, v158 src0_sel:BYTE_1
	v_cvt_f32_fp8_sdwa v83, v158 src0_sel:BYTE_2
	v_cvt_f32_fp8_sdwa v79, v158 src0_sel:BYTE_3
	v_mul_f32_e32 v86, v78, v78
	v_mul_f32_e32 v87, v79, v79
	v_cvt_f32_fp8_e32 v84, v159
	v_cvt_f32_fp8_sdwa v80, v159 src0_sel:BYTE_1
	v_fmac_f32_e32 v86, v82, v82
	v_fmac_f32_e32 v87, v83, v83
	v_add_f32_e32 v86, v86, v87
	v_mul_f32_e32 v87, v80, v80
	v_cvt_f32_fp8_sdwa v85, v159 src0_sel:BYTE_2
	v_cvt_f32_fp8_sdwa v81, v159 src0_sel:BYTE_3
	v_fmac_f32_e32 v87, v84, v84
	v_add_f32_e32 v86, v86, v87
	v_mul_f32_e32 v87, v81, v81
	v_fmac_f32_e32 v87, v85, v85
	v_add_f32_e32 v86, v86, v87
	s_nop 1
	v_add_f32_dpp v86, v86, v86 quad_perm:[1,0,3,2] row_mask:0xf bank_mask:0xf
	s_nop 1
	v_add_f32_dpp v86, v86, v86 quad_perm:[2,3,0,1] row_mask:0xf bank_mask:0xf
	s_nop 1
	v_add_f32_dpp v86, v86, v86 row_half_mirror row_mask:0xf bank_mask:0xf
	s_nop 1
	s_waitcnt lgkmcnt(0)
	v_add_f32_dpp v86, v86, v86 row_mirror row_mask:0xf bank_mask:0xf
	v_fmamk_f32 v86, v86, 0x3c000000, v167
	v_rsq_f32_e32 v86, v86
	s_nop 0
	v_mul_f32_e32 v82, v86, v82
	v_mul_f32_e32 v78, v86, v78
	v_mul_f32_e32 v82, v150, v82
	v_mul_f32_e32 v78, v151, v78
	v_cvt_pk_bf16_f32 v78, v82, v78
	v_mul_f32_e32 v82, v86, v83
	v_mul_f32_e32 v79, v86, v79
	v_mul_f32_e32 v82, v152, v82
	v_mul_f32_e32 v79, v153, v79
	v_cvt_pk_bf16_f32 v79, v82, v79
	v_mul_f32_e32 v82, v86, v84
	v_mul_f32_e32 v80, v86, v80
	v_mul_f32_e32 v82, v146, v82
	v_mul_f32_e32 v80, v147, v80
	v_cvt_pk_bf16_f32 v80, v82, v80
	v_mul_f32_e32 v82, v86, v85
	v_mul_f32_e32 v81, v86, v81
	v_mul_f32_e32 v82, v148, v82
	v_mul_f32_e32 v81, v149, v81
	v_cvt_pk_bf16_f32 v81, v82, v81
	v_add_u32_e32 v82, s1, v180
	ds_write_b128 v82, v[66:69]
	v_add_u32_e32 v66, s1, v181
	ds_write_b128 v66, v[70:73]
	v_add_u32_e32 v66, s1, v196
	ds_write_b128 v66, v[74:77] offset:32768
	v_add_u32_e32 v66, s1, v198
	ds_write_b128 v66, v[78:81] offset:32768
	s_waitcnt lgkmcnt(0)
	s_barrier
	s_cbranch_scc1 .Lna_done
	v_mov_b32_e32 v200, v0
	s_branch .LBB0_469
.Lna_skip:
	s_waitcnt vmcnt(3)
	v_cvt_f32_fp8_e32 v66, v164
	v_cvt_f32_fp8_sdwa v67, v164 src0_sel:BYTE_1
	s_waitcnt vmcnt(0)
	v_cvt_pk_bf16_f32 v66, v66, v67
	v_cvt_f32_fp8_sdwa v67, v164 src0_sel:BYTE_2
	v_cvt_f32_fp8_sdwa v68, v164 src0_sel:BYTE_3
	v_cvt_pk_bf16_f32 v67, v67, v68
	v_cvt_f32_fp8_e32 v68, v165
	v_cvt_f32_fp8_sdwa v69, v165 src0_sel:BYTE_1
	v_cvt_pk_bf16_f32 v68, v68, v69
	v_cvt_f32_fp8_sdwa v69, v165 src0_sel:BYTE_2
	v_cvt_f32_fp8_sdwa v70, v165 src0_sel:BYTE_3
	v_cvt_pk_bf16_f32 v69, v69, v70
	s_waitcnt vmcnt(2)
	v_cvt_f32_fp8_e32 v70, v162
	v_cvt_f32_fp8_sdwa v71, v162 src0_sel:BYTE_1
	v_cvt_pk_bf16_f32 v70, v70, v71
	v_cvt_f32_fp8_sdwa v71, v162 src0_sel:BYTE_2
	v_cvt_f32_fp8_sdwa v72, v162 src0_sel:BYTE_3
	v_cvt_pk_bf16_f32 v71, v71, v72
	v_cvt_f32_fp8_e32 v72, v163
	v_cvt_f32_fp8_sdwa v73, v163 src0_sel:BYTE_1
	v_cvt_pk_bf16_f32 v72, v72, v73
	v_cvt_f32_fp8_sdwa v73, v163 src0_sel:BYTE_2
	v_cvt_f32_fp8_sdwa v74, v163 src0_sel:BYTE_3
	v_cvt_pk_bf16_f32 v73, v73, v74
	s_waitcnt vmcnt(1)
	s_waitcnt vmcnt(0)
	v_cvt_f32_fp8_e32 v82, v160
	v_cvt_f32_fp8_sdwa v74, v160 src0_sel:BYTE_1
	v_cvt_f32_fp8_sdwa v83, v160 src0_sel:BYTE_2
	v_cvt_f32_fp8_sdwa v75, v160 src0_sel:BYTE_3
	v_mul_f32_e32 v86, v74, v74
	v_mul_f32_e32 v87, v75, v75
	v_cvt_f32_fp8_e32 v84, v161
	v_cvt_f32_fp8_sdwa v76, v161 src0_sel:BYTE_1
	v_fmac_f32_e32 v86, v82, v82
	v_fmac_f32_e32 v87, v83, v83
	v_add_f32_e32 v86, v86, v87
	v_mul_f32_e32 v87, v76, v76
	v_cvt_f32_fp8_sdwa v85, v161 src0_sel:BYTE_2
	v_cvt_f32_fp8_sdwa v77, v161 src0_sel:BYTE_3
	v_fmac_f32_e32 v87, v84, v84
	v_add_f32_e32 v86, v86, v87
	v_mul_f32_e32 v87, v77, v77
	v_fmac_f32_e32 v87, v85, v85
	v_add_f32_e32 v86, v86, v87
	s_nop 1
	s_xor_b32 s1, s1, 0x4000
	s_add_i32 s1, s1, 0
	s_add_i32 s92, s92, 1
	s_addk_i32 s3, 0x4000
	v_add_f32_dpp v86, v86, v86 quad_perm:[1,0,3,2] row_mask:0xf bank_mask:0xf
	s_nop 1
	s_add_u32 s96, s96, 0x2000
	s_addc_u32 s97, s97, 0
	s_cmp_eq_u32 s96, 0x18000
	v_add_f32_dpp v86, v86, v86 quad_perm:[2,3,0,1] row_mask:0xf bank_mask:0xf
	s_nop 1
	v_add_f32_dpp v86, v86, v86 row_half_mirror row_mask:0xf bank_mask:0xf
	s_nop 1
	s_waitcnt lgkmcnt(0)
	v_add_f32_dpp v86, v86, v86 row_mirror row_mask:0xf bank_mask:0xf
	v_fmamk_f32 v86, v86, 0x3c000000, v167
	v_rsq_f32_e32 v86, v86
	s_nop 0
	v_mul_f32_e32 v82, v86, v82
	v_mul_f32_e32 v74, v86, v74
	v_mul_f32_e32 v82, v150, v82
	v_mul_f32_e32 v74, v151, v74
	v_cvt_pk_bf16_f32 v74, v82, v74
	v_mul_f32_e32 v82, v86, v83
	v_mul_f32_e32 v75, v86, v75
	v_mul_f32_e32 v82, v152, v82
	v_mul_f32_e32 v75, v153, v75
	v_cvt_pk_bf16_f32 v75, v82, v75
	v_mul_f32_e32 v82, v86, v84
	v_mul_f32_e32 v76, v86, v76
	v_mul_f32_e32 v82, v146, v82
	v_mul_f32_e32 v76, v147, v76
	v_cvt_pk_bf16_f32 v76, v82, v76
	v_mul_f32_e32 v82, v86, v85
	v_mul_f32_e32 v77, v86, v77
	v_mul_f32_e32 v82, v148, v82
	v_mul_f32_e32 v77, v149, v77
	v_cvt_pk_bf16_f32 v77, v82, v77
	v_cvt_f32_fp8_e32 v82, v158
	v_cvt_f32_fp8_sdwa v78, v158 src0_sel:BYTE_1
	v_cvt_f32_fp8_sdwa v83, v158 src0_sel:BYTE_2
	v_cvt_f32_fp8_sdwa v79, v158 src0_sel:BYTE_3
	v_mul_f32_e32 v86, v78, v78
	v_mul_f32_e32 v87, v79, v79
	v_cvt_f32_fp8_e32 v84, v159
	v_cvt_f32_fp8_sdwa v80, v159 src0_sel:BYTE_1
	v_fmac_f32_e32 v86, v82, v82
	v_fmac_f32_e32 v87, v83, v83
	v_add_f32_e32 v86, v86, v87
	v_mul_f32_e32 v87, v80, v80
	v_cvt_f32_fp8_sdwa v85, v159 src0_sel:BYTE_2
	v_cvt_f32_fp8_sdwa v81, v159 src0_sel:BYTE_3
	v_fmac_f32_e32 v87, v84, v84
	v_add_f32_e32 v86, v86, v87
	v_mul_f32_e32 v87, v81, v81
	v_fmac_f32_e32 v87, v85, v85
	v_add_f32_e32 v86, v86, v87
	s_nop 1
	v_add_f32_dpp v86, v86, v86 quad_perm:[1,0,3,2] row_mask:0xf bank_mask:0xf
	s_nop 1
	v_add_f32_dpp v86, v86, v86 quad_perm:[2,3,0,1] row_mask:0xf bank_mask:0xf
	s_nop 1
	v_add_f32_dpp v86, v86, v86 row_half_mirror row_mask:0xf bank_mask:0xf
	s_nop 1
	s_waitcnt lgkmcnt(0)
	v_add_f32_dpp v86, v86, v86 row_mirror row_mask:0xf bank_mask:0xf
	v_fmamk_f32 v86, v86, 0x3c000000, v167
	v_rsq_f32_e32 v86, v86
	s_nop 0
	v_mul_f32_e32 v82, v86, v82
	v_mul_f32_e32 v78, v86, v78
	v_mul_f32_e32 v82, v150, v82
	v_mul_f32_e32 v78, v151, v78
	v_cvt_pk_bf16_f32 v78, v82, v78
	v_mul_f32_e32 v82, v86, v83
	v_mul_f32_e32 v79, v86, v79
	v_mul_f32_e32 v82, v152, v82
	v_mul_f32_e32 v79, v153, v79
	v_cvt_pk_bf16_f32 v79, v82, v79
	v_mul_f32_e32 v82, v86, v84
	v_mul_f32_e32 v80, v86, v80
	v_mul_f32_e32 v82, v146, v82
	v_mul_f32_e32 v80, v147, v80
	v_cvt_pk_bf16_f32 v80, v82, v80
	v_mul_f32_e32 v82, v86, v85
	v_mul_f32_e32 v81, v86, v81
	v_mul_f32_e32 v82, v148, v82
	v_mul_f32_e32 v81, v149, v81
	v_cvt_pk_bf16_f32 v81, v82, v81
	v_add_u32_e32 v82, s1, v180
	ds_write_b128 v82, v[66:69]
	v_add_u32_e32 v66, s1, v181
	ds_write_b128 v66, v[70:73]
	v_add_u32_e32 v66, s1, v196
	ds_write_b128 v66, v[74:77] offset:32768
	v_add_u32_e32 v66, s1, v198
	ds_write_b128 v66, v[78:81] offset:32768
	v_mov_b32_e32 v0, v200
	s_waitcnt lgkmcnt(0)
	s_barrier
	s_cbranch_scc1 .Lna_done
	s_branch .LBB0_469
.Lna_done:
	v_readlane_b32 s96, v252, 26
	v_readlane_b32 s97, v252, 27
	v_readlane_b32 s64, v252, 7
	v_readlane_b32 s65, v252, 8
	s_and_saveexec_b64 s[6:7], s[4:5]
	ds_write_b32 v179, v0
	s_branch .LBB0_463
